# expert gate/up (silu*up -> e4m3) epilogue rewritten in both MoE layers: packed scale/add around exp and rcp, 16-byte stores via lane-pair exchange, 32-bit offsets
# speedup vs baseline: 1.0058x; 1.0058x over previous
; DI float silu_f(float a) { return a * __builtin_amdgcn_rcpf(1.0f + __expf(-a)); }
;     DI void operator()(const f32x4 (&acc)[2][2][4][2], const Unit& u, int wr, int wc, int fr, int fq) const {
;         const int row0 = u.pm * 256 + wr * 64 + fr, col0 = (u.pn % pn_mod) * 128 + wc * 32 + 8 * fq;
; #pragma unroll
;         for (int ai = 0; ai < 2; ++ai)
; #pragma unroll
;             for (int m = 0; m < 4; ++m) {
;                 unsigned char* rowp = O + (size_t)(row0 + ai * 128 + m * 16) * ldc + col0;
;                 f32x4 a0 = acc[ai][0][m][0] * W8_INV, a1 = acc[ai][0][m][1] * W8_INV; const f32x4 b0 = acc[ai][1][m][0] * W8_INV, b1 = acc[ai][1][m][1] * W8_INV;
; #pragma unroll
;                 for (int j = 0; j < 4; ++j) { a0[j] = silu_f(a0[j]); a1[j] = silu_f(a1[j]); }
;                 const f32x4 v0 = a0 * b0, v1 = a1 * b1;
;                 u32x2 w; w.x = pk4_fp8(v0[0], v0[1], v0[2], v0[3]); w.y = pk4_fp8(v1[0], v1[1], v1[2], v1[3]);
;                 *(u32x2*)rowp = w;
;             }
;     }
.LBB0_846:
	s_mov_b32 vcc_lo, 0xbfb8aa3b
	s_mov_b32 vcc_hi, 1.0
	v_and_b32_e32 v14, 8, v214
	v_lshlrev_b32_e32 v14, 1, v14
	v_add_u32_e32 v14, v14, v205
	v_lshl_add_u32 v14, s58, 8, v14
	v_lshlrev_b32_e32 v15, 10, v14
	s_and_b32 s11, s16, 7
	s_lshl_b32 s11, s11, 7
	v_and_b32_e32 v14, 0x70, v214
	v_or_b32_e32 v14, s11, v14
	v_add_u32_e32 v15, v15, v14
	v_pk_mul_f32 v[190:191], v[190:191], s[8:9] op_sel_hi:[1,0]
	v_pk_mul_f32 v[192:193], v[192:193], s[8:9] op_sel_hi:[1,0]
	v_pk_mul_f32 v[186:187], v[186:187], s[8:9] op_sel_hi:[1,0]
	v_pk_mul_f32 v[188:189], v[188:189], s[8:9] op_sel_hi:[1,0]
	v_pk_mul_f32 v[182:183], v[182:183], s[8:9] op_sel_hi:[1,0]
	v_pk_mul_f32 v[184:185], v[184:185], s[8:9] op_sel_hi:[1,0]
	v_pk_mul_f32 v[178:179], v[178:179], s[8:9] op_sel_hi:[1,0]
	v_pk_mul_f32 v[180:181], v[180:181], s[8:9] op_sel_hi:[1,0]
	v_pk_mul_f32 v[2:3], v[190:191], vcc op_sel_hi:[1,0]
	v_pk_mul_f32 v[4:5], v[192:193], vcc op_sel_hi:[1,0]
	v_pk_mul_f32 v[6:7], v[186:187], vcc op_sel_hi:[1,0]
	v_pk_mul_f32 v[8:9], v[188:189], vcc op_sel_hi:[1,0]
	v_exp_f32_e32 v2, v2
	v_exp_f32_e32 v3, v3
	v_exp_f32_e32 v4, v4
	v_exp_f32_e32 v5, v5
	v_exp_f32_e32 v6, v6
	v_exp_f32_e32 v7, v7
	v_exp_f32_e32 v8, v8
	v_exp_f32_e32 v9, v9
	v_pk_add_f32 v[2:3], v[2:3], vcc op_sel:[0,1] op_sel_hi:[1,1]
	v_pk_add_f32 v[4:5], v[4:5], vcc op_sel:[0,1] op_sel_hi:[1,1]
	v_pk_add_f32 v[6:7], v[6:7], vcc op_sel:[0,1] op_sel_hi:[1,1]
	v_pk_add_f32 v[8:9], v[8:9], vcc op_sel:[0,1] op_sel_hi:[1,1]
	v_rcp_f32_e32 v2, v2
	v_rcp_f32_e32 v3, v3
	v_rcp_f32_e32 v4, v4
	v_rcp_f32_e32 v5, v5
	v_rcp_f32_e32 v6, v6
	v_rcp_f32_e32 v7, v7
	v_rcp_f32_e32 v8, v8
	v_rcp_f32_e32 v9, v9
	v_pk_mul_f32 v[190:191], v[190:191], v[2:3]
	v_pk_mul_f32 v[192:193], v[192:193], v[4:5]
	v_pk_mul_f32 v[186:187], v[186:187], v[6:7]
	v_pk_mul_f32 v[188:189], v[188:189], v[8:9]
	v_pk_mul_f32 v[190:191], v[182:183], v[190:191]
	v_pk_mul_f32 v[192:193], v[184:185], v[192:193]
	v_pk_mul_f32 v[186:187], v[178:179], v[186:187]
	v_pk_mul_f32 v[188:189], v[180:181], v[188:189]
	v_med3_f32 v190, v190, s56, v219
	v_med3_f32 v191, v191, s56, v219
	v_med3_f32 v192, v192, s56, v219
	v_med3_f32 v193, v193, s56, v219
	v_med3_f32 v186, v186, s56, v219
	v_med3_f32 v187, v187, s56, v219
	v_med3_f32 v188, v188, s56, v219
	v_med3_f32 v189, v189, s56, v219
	v_cvt_pk_fp8_f32 v10, v190, v191
	v_cvt_pk_fp8_f32 v11, v186, v187
	v_cvt_pk_fp8_f32 v10, v192, v193 op_sel:[0,0,1]
	v_cvt_pk_fp8_f32 v11, v188, v189 op_sel:[0,0,1]
	v_pk_mul_f32 v[174:175], v[174:175], s[8:9] op_sel_hi:[1,0]
	v_pk_mul_f32 v[176:177], v[176:177], s[8:9] op_sel_hi:[1,0]
	v_pk_mul_f32 v[170:171], v[170:171], s[8:9] op_sel_hi:[1,0]
	v_pk_mul_f32 v[172:173], v[172:173], s[8:9] op_sel_hi:[1,0]
	v_pk_mul_f32 v[166:167], v[166:167], s[8:9] op_sel_hi:[1,0]
	v_pk_mul_f32 v[168:169], v[168:169], s[8:9] op_sel_hi:[1,0]
	v_pk_mul_f32 v[162:163], v[162:163], s[8:9] op_sel_hi:[1,0]
	v_pk_mul_f32 v[164:165], v[164:165], s[8:9] op_sel_hi:[1,0]
	v_pk_mul_f32 v[2:3], v[174:175], vcc op_sel_hi:[1,0]
	v_pk_mul_f32 v[4:5], v[176:177], vcc op_sel_hi:[1,0]
	v_pk_mul_f32 v[6:7], v[170:171], vcc op_sel_hi:[1,0]
	v_pk_mul_f32 v[8:9], v[172:173], vcc op_sel_hi:[1,0]
	v_exp_f32_e32 v2, v2
	v_exp_f32_e32 v3, v3
	v_exp_f32_e32 v4, v4
	v_exp_f32_e32 v5, v5
	v_exp_f32_e32 v6, v6
	v_exp_f32_e32 v7, v7
	v_exp_f32_e32 v8, v8
	v_exp_f32_e32 v9, v9
	v_pk_add_f32 v[2:3], v[2:3], vcc op_sel:[0,1] op_sel_hi:[1,1]
	v_pk_add_f32 v[4:5], v[4:5], vcc op_sel:[0,1] op_sel_hi:[1,1]
	v_pk_add_f32 v[6:7], v[6:7], vcc op_sel:[0,1] op_sel_hi:[1,1]
	v_pk_add_f32 v[8:9], v[8:9], vcc op_sel:[0,1] op_sel_hi:[1,1]
	v_rcp_f32_e32 v2, v2
	v_rcp_f32_e32 v3, v3
	v_rcp_f32_e32 v4, v4
	v_rcp_f32_e32 v5, v5
	v_rcp_f32_e32 v6, v6
	v_rcp_f32_e32 v7, v7
	v_rcp_f32_e32 v8, v8
	v_rcp_f32_e32 v9, v9
	v_pk_mul_f32 v[174:175], v[174:175], v[2:3]
	v_pk_mul_f32 v[176:177], v[176:177], v[4:5]
	v_pk_mul_f32 v[170:171], v[170:171], v[6:7]
	v_pk_mul_f32 v[172:173], v[172:173], v[8:9]
	v_pk_mul_f32 v[174:175], v[166:167], v[174:175]
	v_pk_mul_f32 v[176:177], v[168:169], v[176:177]
	v_pk_mul_f32 v[170:171], v[162:163], v[170:171]
	v_pk_mul_f32 v[172:173], v[164:165], v[172:173]
	v_med3_f32 v174, v174, s56, v219
	v_med3_f32 v175, v175, s56, v219
	v_med3_f32 v176, v176, s56, v219
	v_med3_f32 v177, v177, s56, v219
	v_med3_f32 v170, v170, s56, v219
	v_med3_f32 v171, v171, s56, v219
	v_med3_f32 v172, v172, s56, v219
	v_med3_f32 v173, v173, s56, v219
	v_cvt_pk_fp8_f32 v12, v174, v175
	v_cvt_pk_fp8_f32 v13, v170, v171
	v_cvt_pk_fp8_f32 v12, v176, v177 op_sel:[0,0,1]
	v_cvt_pk_fp8_f32 v13, v172, v173 op_sel:[0,0,1]
	s_nop 1
	v_permlane16_swap_b32_e32 v10, v12
	v_permlane16_swap_b32_e32 v11, v13
	v_mov_b32_e32 v14, v15
	global_store_dwordx4 v14, v[10:13], s[94:95]
	v_pk_mul_f32 v[158:159], v[158:159], s[8:9] op_sel_hi:[1,0]
	v_pk_mul_f32 v[160:161], v[160:161], s[8:9] op_sel_hi:[1,0]
	v_pk_mul_f32 v[154:155], v[154:155], s[8:9] op_sel_hi:[1,0]
	v_pk_mul_f32 v[156:157], v[156:157], s[8:9] op_sel_hi:[1,0]
	v_pk_mul_f32 v[150:151], v[150:151], s[8:9] op_sel_hi:[1,0]
	v_pk_mul_f32 v[152:153], v[152:153], s[8:9] op_sel_hi:[1,0]
	v_pk_mul_f32 v[146:147], v[146:147], s[8:9] op_sel_hi:[1,0]
	v_pk_mul_f32 v[148:149], v[148:149], s[8:9] op_sel_hi:[1,0]
	v_pk_mul_f32 v[2:3], v[158:159], vcc op_sel_hi:[1,0]
	v_pk_mul_f32 v[4:5], v[160:161], vcc op_sel_hi:[1,0]
	v_pk_mul_f32 v[6:7], v[154:155], vcc op_sel_hi:[1,0]
	v_pk_mul_f32 v[8:9], v[156:157], vcc op_sel_hi:[1,0]
	v_exp_f32_e32 v2, v2
	v_exp_f32_e32 v3, v3
	v_exp_f32_e32 v4, v4
	v_exp_f32_e32 v5, v5
	v_exp_f32_e32 v6, v6
	v_exp_f32_e32 v7, v7
	v_exp_f32_e32 v8, v8
	v_exp_f32_e32 v9, v9
; DI float silu_f(float a) { return a * __builtin_amdgcn_rcpf(1.0f + __expf(-a)); }
;     DI void operator()(const f32x4 (&acc)[2][2][4][2], const Unit& u, int wr, int wc, int fr, int fq) const {
;         const int row0 = u.pm * 256 + wr * 64 + fr, col0 = (u.pn % pn_mod) * 128 + wc * 32 + 8 * fq;
; #pragma unroll
;         for (int ai = 0; ai < 2; ++ai)
; #pragma unroll
;             for (int m = 0; m < 4; ++m) {
;                 unsigned char* rowp = O + (size_t)(row0 + ai * 128 + m * 16) * ldc + col0;
;                 f32x4 a0 = acc[ai][0][m][0] * W8_INV, a1 = acc[ai][0][m][1] * W8_INV; const f32x4 b0 = acc[ai][1][m][0] * W8_INV, b1 = acc[ai][1][m][1] * W8_INV;
; #pragma unroll
;                 for (int j = 0; j < 4; ++j) { a0[j] = silu_f(a0[j]); a1[j] = silu_f(a1[j]); }
;                 const f32x4 v0 = a0 * b0, v1 = a1 * b1;
;                 u32x2 w; w.x = pk4_fp8(v0[0], v0[1], v0[2], v0[3]); w.y = pk4_fp8(v1[0], v1[1], v1[2], v1[3]);
;                 *(u32x2*)rowp = w;
;             }
;     }
	v_pk_add_f32 v[2:3], v[2:3], vcc op_sel:[0,1] op_sel_hi:[1,1]
	v_pk_add_f32 v[4:5], v[4:5], vcc op_sel:[0,1] op_sel_hi:[1,1]
	v_pk_add_f32 v[6:7], v[6:7], vcc op_sel:[0,1] op_sel_hi:[1,1]
	v_pk_add_f32 v[8:9], v[8:9], vcc op_sel:[0,1] op_sel_hi:[1,1]
	v_rcp_f32_e32 v2, v2
	v_rcp_f32_e32 v3, v3
	v_rcp_f32_e32 v4, v4
	v_rcp_f32_e32 v5, v5
	v_rcp_f32_e32 v6, v6
	v_rcp_f32_e32 v7, v7
	v_rcp_f32_e32 v8, v8
	v_rcp_f32_e32 v9, v9
	v_pk_mul_f32 v[158:159], v[158:159], v[2:3]
	v_pk_mul_f32 v[160:161], v[160:161], v[4:5]
	v_pk_mul_f32 v[154:155], v[154:155], v[6:7]
	v_pk_mul_f32 v[156:157], v[156:157], v[8:9]
	v_pk_mul_f32 v[158:159], v[150:151], v[158:159]
	v_pk_mul_f32 v[160:161], v[152:153], v[160:161]
	v_pk_mul_f32 v[154:155], v[146:147], v[154:155]
	v_pk_mul_f32 v[156:157], v[148:149], v[156:157]
	v_med3_f32 v158, v158, s56, v219
	v_med3_f32 v159, v159, s56, v219
	v_med3_f32 v160, v160, s56, v219
	v_med3_f32 v161, v161, s56, v219
	v_med3_f32 v154, v154, s56, v219
	v_med3_f32 v155, v155, s56, v219
	v_med3_f32 v156, v156, s56, v219
	v_med3_f32 v157, v157, s56, v219
	v_cvt_pk_fp8_f32 v16, v158, v159
	v_cvt_pk_fp8_f32 v17, v154, v155
	v_cvt_pk_fp8_f32 v16, v160, v161 op_sel:[0,0,1]
	v_cvt_pk_fp8_f32 v17, v156, v157 op_sel:[0,0,1]
	v_pk_mul_f32 v[142:143], v[142:143], s[8:9] op_sel_hi:[1,0]
	v_pk_mul_f32 v[144:145], v[144:145], s[8:9] op_sel_hi:[1,0]
	v_pk_mul_f32 v[138:139], v[138:139], s[8:9] op_sel_hi:[1,0]
	v_pk_mul_f32 v[140:141], v[140:141], s[8:9] op_sel_hi:[1,0]
	v_pk_mul_f32 v[134:135], v[134:135], s[8:9] op_sel_hi:[1,0]
	v_pk_mul_f32 v[136:137], v[136:137], s[8:9] op_sel_hi:[1,0]
	v_pk_mul_f32 v[130:131], v[130:131], s[8:9] op_sel_hi:[1,0]
	v_pk_mul_f32 v[132:133], v[132:133], s[8:9] op_sel_hi:[1,0]
	v_pk_mul_f32 v[2:3], v[142:143], vcc op_sel_hi:[1,0]
	v_pk_mul_f32 v[4:5], v[144:145], vcc op_sel_hi:[1,0]
	v_pk_mul_f32 v[6:7], v[138:139], vcc op_sel_hi:[1,0]
	v_pk_mul_f32 v[8:9], v[140:141], vcc op_sel_hi:[1,0]
	v_exp_f32_e32 v2, v2
	v_exp_f32_e32 v3, v3
	v_exp_f32_e32 v4, v4
	v_exp_f32_e32 v5, v5
	v_exp_f32_e32 v6, v6
	v_exp_f32_e32 v7, v7
	v_exp_f32_e32 v8, v8
	v_exp_f32_e32 v9, v9
	v_pk_add_f32 v[2:3], v[2:3], vcc op_sel:[0,1] op_sel_hi:[1,1]
	v_pk_add_f32 v[4:5], v[4:5], vcc op_sel:[0,1] op_sel_hi:[1,1]
	v_pk_add_f32 v[6:7], v[6:7], vcc op_sel:[0,1] op_sel_hi:[1,1]
	v_pk_add_f32 v[8:9], v[8:9], vcc op_sel:[0,1] op_sel_hi:[1,1]
	v_rcp_f32_e32 v2, v2
	v_rcp_f32_e32 v3, v3
	v_rcp_f32_e32 v4, v4
	v_rcp_f32_e32 v5, v5
	v_rcp_f32_e32 v6, v6
	v_rcp_f32_e32 v7, v7
	v_rcp_f32_e32 v8, v8
	v_rcp_f32_e32 v9, v9
	v_pk_mul_f32 v[142:143], v[142:143], v[2:3]
	v_pk_mul_f32 v[144:145], v[144:145], v[4:5]
	v_pk_mul_f32 v[138:139], v[138:139], v[6:7]
	v_pk_mul_f32 v[140:141], v[140:141], v[8:9]
	v_pk_mul_f32 v[142:143], v[134:135], v[142:143]
	v_pk_mul_f32 v[144:145], v[136:137], v[144:145]
	v_pk_mul_f32 v[138:139], v[130:131], v[138:139]
	v_pk_mul_f32 v[140:141], v[132:133], v[140:141]
	v_med3_f32 v142, v142, s56, v219
	v_med3_f32 v143, v143, s56, v219
	v_med3_f32 v144, v144, s56, v219
	v_med3_f32 v145, v145, s56, v219
	v_med3_f32 v138, v138, s56, v219
	v_med3_f32 v139, v139, s56, v219
	v_med3_f32 v140, v140, s56, v219
	v_med3_f32 v141, v141, s56, v219
	v_cvt_pk_fp8_f32 v18, v142, v143
	v_cvt_pk_fp8_f32 v19, v138, v139
	v_cvt_pk_fp8_f32 v18, v144, v145 op_sel:[0,0,1]
	v_cvt_pk_fp8_f32 v19, v140, v141 op_sel:[0,0,1]
	s_nop 1
	v_permlane16_swap_b32_e32 v16, v18
	v_permlane16_swap_b32_e32 v17, v19
	v_add_u32_e32 v14, 0x8000, v15
	global_store_dwordx4 v14, v[16:19], s[94:95]
	v_pk_mul_f32 v[126:127], v[126:127], s[8:9] op_sel_hi:[1,0]
	v_pk_mul_f32 v[128:129], v[128:129], s[8:9] op_sel_hi:[1,0]
	v_pk_mul_f32 v[122:123], v[122:123], s[8:9] op_sel_hi:[1,0]
	v_pk_mul_f32 v[124:125], v[124:125], s[8:9] op_sel_hi:[1,0]
	v_pk_mul_f32 v[118:119], v[118:119], s[8:9] op_sel_hi:[1,0]
	v_pk_mul_f32 v[120:121], v[120:121], s[8:9] op_sel_hi:[1,0]
	v_pk_mul_f32 v[114:115], v[114:115], s[8:9] op_sel_hi:[1,0]
	v_pk_mul_f32 v[116:117], v[116:117], s[8:9] op_sel_hi:[1,0]
	v_pk_mul_f32 v[2:3], v[126:127], vcc op_sel_hi:[1,0]
	v_pk_mul_f32 v[4:5], v[128:129], vcc op_sel_hi:[1,0]
	v_pk_mul_f32 v[6:7], v[122:123], vcc op_sel_hi:[1,0]
	v_pk_mul_f32 v[8:9], v[124:125], vcc op_sel_hi:[1,0]
	v_exp_f32_e32 v2, v2
	v_exp_f32_e32 v3, v3
	v_exp_f32_e32 v4, v4
	v_exp_f32_e32 v5, v5
	v_exp_f32_e32 v6, v6
	v_exp_f32_e32 v7, v7
	v_exp_f32_e32 v8, v8
	v_exp_f32_e32 v9, v9
	v_pk_add_f32 v[2:3], v[2:3], vcc op_sel:[0,1] op_sel_hi:[1,1]
	v_pk_add_f32 v[4:5], v[4:5], vcc op_sel:[0,1] op_sel_hi:[1,1]
	v_pk_add_f32 v[6:7], v[6:7], vcc op_sel:[0,1] op_sel_hi:[1,1]
	v_pk_add_f32 v[8:9], v[8:9], vcc op_sel:[0,1] op_sel_hi:[1,1]
	v_rcp_f32_e32 v2, v2
	v_rcp_f32_e32 v3, v3
	v_rcp_f32_e32 v4, v4
	v_rcp_f32_e32 v5, v5
	v_rcp_f32_e32 v6, v6
	v_rcp_f32_e32 v7, v7
	v_rcp_f32_e32 v8, v8
	v_rcp_f32_e32 v9, v9
	v_pk_mul_f32 v[126:127], v[126:127], v[2:3]
	v_pk_mul_f32 v[128:129], v[128:129], v[4:5]
	v_pk_mul_f32 v[122:123], v[122:123], v[6:7]
	v_pk_mul_f32 v[124:125], v[124:125], v[8:9]
	v_pk_mul_f32 v[126:127], v[118:119], v[126:127]
	v_pk_mul_f32 v[128:129], v[120:121], v[128:129]
	v_pk_mul_f32 v[122:123], v[114:115], v[122:123]
	v_pk_mul_f32 v[124:125], v[116:117], v[124:125]
	v_med3_f32 v126, v126, s56, v219
	v_med3_f32 v127, v127, s56, v219
	v_med3_f32 v128, v128, s56, v219
	v_med3_f32 v129, v129, s56, v219
	v_med3_f32 v122, v122, s56, v219
	v_med3_f32 v123, v123, s56, v219
	v_med3_f32 v124, v124, s56, v219
	v_med3_f32 v125, v125, s56, v219
	v_cvt_pk_fp8_f32 v10, v126, v127
	v_cvt_pk_fp8_f32 v11, v122, v123
	v_cvt_pk_fp8_f32 v10, v128, v129 op_sel:[0,0,1]
	v_cvt_pk_fp8_f32 v11, v124, v125 op_sel:[0,0,1]
; #define PG8_BAR __builtin_amdgcn_s_barrier()
; DI float silu_f(float a) { return a * __builtin_amdgcn_rcpf(1.0f + __expf(-a)); }
; template <class Epi, class Sched, bool ALIGN_EPI = false, bool SP2 = false, bool GATHER = false, bool F8 = false>
; __device__ __forceinline__ void gemm_phase(PG8_LAS unsigned char* lds, const Gemm g, const Sched& S, const Epi& E) {
;     ...
;         if constexpr (ALIGN_EPI) { if (wr == 0) PG8_BAR; }
;         if constexpr (!Epi::AFTER_DRAIN) { E(acc, cur, wr, wc, fr, fq); S.done(cur); }
;         if (!has_next) break;
; #pragma unroll
;         for (int a = 0; a < 2; ++a)
; #pragma unroll
;             for (int b = 0; b < 2; ++b)
; #pragma unroll
;                 for (int m = 0; m < 4; ++m)
; #pragma unroll
;                     for (int n = 0; n < 2; ++n) acc[a][b][m][n] = (f32x4){0.f, 0.f, 0.f, 0.f};
;         cur = nxt; cA = nA; cB = nB; ++ui;
;         if constexpr (ALIGN_EPI) { if (wr == 1) PG8_BAR; }
;     DI void operator()(const f32x4 (&acc)[2][2][4][2], const Unit& u, int wr, int wc, int fr, int fq) const {
;         const int row0 = u.pm * 256 + wr * 64 + fr, col0 = (u.pn % pn_mod) * 128 + wc * 32 + 8 * fq;
; #pragma unroll
;         for (int ai = 0; ai < 2; ++ai)
; #pragma unroll
;             for (int m = 0; m < 4; ++m) {
;                 unsigned char* rowp = O + (size_t)(row0 + ai * 128 + m * 16) * ldc + col0;
;                 f32x4 a0 = acc[ai][0][m][0] * W8_INV, a1 = acc[ai][0][m][1] * W8_INV; const f32x4 b0 = acc[ai][1][m][0] * W8_INV, b1 = acc[ai][1][m][1] * W8_INV;
; #pragma unroll
;                 for (int j = 0; j < 4; ++j) { a0[j] = silu_f(a0[j]); a1[j] = silu_f(a1[j]); }
;                 const f32x4 v0 = a0 * b0, v1 = a1 * b1;
;                 u32x2 w; w.x = pk4_fp8(v0[0], v0[1], v0[2], v0[3]); w.y = pk4_fp8(v1[0], v1[1], v1[2], v1[3]);
;                 *(u32x2*)rowp = w;
;             }
;     }
	v_pk_mul_f32 v[110:111], v[110:111], s[8:9] op_sel_hi:[1,0]
	v_pk_mul_f32 v[112:113], v[112:113], s[8:9] op_sel_hi:[1,0]
	v_pk_mul_f32 v[106:107], v[106:107], s[8:9] op_sel_hi:[1,0]
	v_pk_mul_f32 v[108:109], v[108:109], s[8:9] op_sel_hi:[1,0]
	v_pk_mul_f32 v[94:95], v[94:95], s[8:9] op_sel_hi:[1,0]
	v_pk_mul_f32 v[96:97], v[96:97], s[8:9] op_sel_hi:[1,0]
	v_pk_mul_f32 v[90:91], v[90:91], s[8:9] op_sel_hi:[1,0]
	v_pk_mul_f32 v[92:93], v[92:93], s[8:9] op_sel_hi:[1,0]
	v_pk_mul_f32 v[2:3], v[110:111], vcc op_sel_hi:[1,0]
	v_pk_mul_f32 v[4:5], v[112:113], vcc op_sel_hi:[1,0]
	v_pk_mul_f32 v[6:7], v[106:107], vcc op_sel_hi:[1,0]
	v_pk_mul_f32 v[8:9], v[108:109], vcc op_sel_hi:[1,0]
	v_exp_f32_e32 v2, v2
	v_exp_f32_e32 v3, v3
	v_exp_f32_e32 v4, v4
	v_exp_f32_e32 v5, v5
	v_exp_f32_e32 v6, v6
	v_exp_f32_e32 v7, v7
	v_exp_f32_e32 v8, v8
	v_exp_f32_e32 v9, v9
	v_pk_add_f32 v[2:3], v[2:3], vcc op_sel:[0,1] op_sel_hi:[1,1]
	v_pk_add_f32 v[4:5], v[4:5], vcc op_sel:[0,1] op_sel_hi:[1,1]
	v_pk_add_f32 v[6:7], v[6:7], vcc op_sel:[0,1] op_sel_hi:[1,1]
	v_pk_add_f32 v[8:9], v[8:9], vcc op_sel:[0,1] op_sel_hi:[1,1]
	v_rcp_f32_e32 v2, v2
	v_rcp_f32_e32 v3, v3
	v_rcp_f32_e32 v4, v4
	v_rcp_f32_e32 v5, v5
	v_rcp_f32_e32 v6, v6
	v_rcp_f32_e32 v7, v7
	v_rcp_f32_e32 v8, v8
	v_rcp_f32_e32 v9, v9
	v_pk_mul_f32 v[110:111], v[110:111], v[2:3]
	v_pk_mul_f32 v[112:113], v[112:113], v[4:5]
	v_pk_mul_f32 v[106:107], v[106:107], v[6:7]
	v_pk_mul_f32 v[108:109], v[108:109], v[8:9]
	v_pk_mul_f32 v[110:111], v[94:95], v[110:111]
	v_pk_mul_f32 v[112:113], v[96:97], v[112:113]
	v_pk_mul_f32 v[106:107], v[90:91], v[106:107]
	v_pk_mul_f32 v[108:109], v[92:93], v[108:109]
	v_med3_f32 v110, v110, s56, v219
	v_med3_f32 v111, v111, s56, v219
	v_med3_f32 v112, v112, s56, v219
	v_med3_f32 v113, v113, s56, v219
	v_med3_f32 v106, v106, s56, v219
	v_med3_f32 v107, v107, s56, v219
	v_med3_f32 v108, v108, s56, v219
	v_med3_f32 v109, v109, s56, v219
	v_cvt_pk_fp8_f32 v12, v110, v111
	v_cvt_pk_fp8_f32 v13, v106, v107
	v_cvt_pk_fp8_f32 v12, v112, v113 op_sel:[0,0,1]
	v_cvt_pk_fp8_f32 v13, v108, v109 op_sel:[0,0,1]
	s_nop 1
	v_permlane16_swap_b32_e32 v10, v12
	v_permlane16_swap_b32_e32 v11, v13
	v_add_u32_e32 v14, 0x20000, v15
	global_store_dwordx4 v14, v[10:13], s[94:95]
	v_pk_mul_f32 v[86:87], v[86:87], s[8:9] op_sel_hi:[1,0]
	v_pk_mul_f32 v[88:89], v[88:89], s[8:9] op_sel_hi:[1,0]
	v_pk_mul_f32 v[82:83], v[82:83], s[8:9] op_sel_hi:[1,0]
	v_pk_mul_f32 v[84:85], v[84:85], s[8:9] op_sel_hi:[1,0]
	v_pk_mul_f32 v[98:99], v[98:99], s[8:9] op_sel_hi:[1,0]
	v_pk_mul_f32 v[100:101], v[100:101], s[8:9] op_sel_hi:[1,0]
	v_pk_mul_f32 v[102:103], v[102:103], s[8:9] op_sel_hi:[1,0]
	v_pk_mul_f32 v[104:105], v[104:105], s[8:9] op_sel_hi:[1,0]
	v_pk_mul_f32 v[2:3], v[86:87], vcc op_sel_hi:[1,0]
	v_pk_mul_f32 v[4:5], v[88:89], vcc op_sel_hi:[1,0]
	v_pk_mul_f32 v[6:7], v[82:83], vcc op_sel_hi:[1,0]
	v_pk_mul_f32 v[8:9], v[84:85], vcc op_sel_hi:[1,0]
	v_exp_f32_e32 v2, v2
	v_exp_f32_e32 v3, v3
	v_exp_f32_e32 v4, v4
	v_exp_f32_e32 v5, v5
	v_exp_f32_e32 v6, v6
	v_exp_f32_e32 v7, v7
	v_exp_f32_e32 v8, v8
	v_exp_f32_e32 v9, v9
	v_pk_add_f32 v[2:3], v[2:3], vcc op_sel:[0,1] op_sel_hi:[1,1]
	v_pk_add_f32 v[4:5], v[4:5], vcc op_sel:[0,1] op_sel_hi:[1,1]
	v_pk_add_f32 v[6:7], v[6:7], vcc op_sel:[0,1] op_sel_hi:[1,1]
	v_pk_add_f32 v[8:9], v[8:9], vcc op_sel:[0,1] op_sel_hi:[1,1]
	v_rcp_f32_e32 v2, v2
	v_rcp_f32_e32 v3, v3
	v_rcp_f32_e32 v4, v4
	v_rcp_f32_e32 v5, v5
	v_rcp_f32_e32 v6, v6
	v_rcp_f32_e32 v7, v7
	v_rcp_f32_e32 v8, v8
	v_rcp_f32_e32 v9, v9
	v_pk_mul_f32 v[86:87], v[86:87], v[2:3]
	v_pk_mul_f32 v[88:89], v[88:89], v[4:5]
	v_pk_mul_f32 v[82:83], v[82:83], v[6:7]
	v_pk_mul_f32 v[84:85], v[84:85], v[8:9]
	v_pk_mul_f32 v[86:87], v[98:99], v[86:87]
	v_pk_mul_f32 v[88:89], v[100:101], v[88:89]
	v_pk_mul_f32 v[82:83], v[102:103], v[82:83]
	v_pk_mul_f32 v[84:85], v[104:105], v[84:85]
	v_med3_f32 v86, v86, s56, v219
	v_med3_f32 v87, v87, s56, v219
	v_med3_f32 v88, v88, s56, v219
	v_med3_f32 v89, v89, s56, v219
	v_med3_f32 v82, v82, s56, v219
	v_med3_f32 v83, v83, s56, v219
	v_med3_f32 v84, v84, s56, v219
	v_med3_f32 v85, v85, s56, v219
	v_cvt_pk_fp8_f32 v16, v86, v87
	v_cvt_pk_fp8_f32 v17, v82, v83
	v_cvt_pk_fp8_f32 v16, v88, v89 op_sel:[0,0,1]
	v_cvt_pk_fp8_f32 v17, v84, v85 op_sel:[0,0,1]
	v_pk_mul_f32 v[70:71], v[70:71], s[8:9] op_sel_hi:[1,0]
	v_pk_mul_f32 v[72:73], v[72:73], s[8:9] op_sel_hi:[1,0]
	v_pk_mul_f32 v[66:67], v[66:67], s[8:9] op_sel_hi:[1,0]
	v_pk_mul_f32 v[68:69], v[68:69], s[8:9] op_sel_hi:[1,0]
	v_pk_mul_f32 v[74:75], v[74:75], s[8:9] op_sel_hi:[1,0]
	v_pk_mul_f32 v[76:77], v[76:77], s[8:9] op_sel_hi:[1,0]
	v_pk_mul_f32 v[78:79], v[78:79], s[8:9] op_sel_hi:[1,0]
	v_pk_mul_f32 v[80:81], v[80:81], s[8:9] op_sel_hi:[1,0]
	v_pk_mul_f32 v[2:3], v[70:71], vcc op_sel_hi:[1,0]
	v_pk_mul_f32 v[4:5], v[72:73], vcc op_sel_hi:[1,0]
	v_pk_mul_f32 v[6:7], v[66:67], vcc op_sel_hi:[1,0]
	v_pk_mul_f32 v[8:9], v[68:69], vcc op_sel_hi:[1,0]
	v_exp_f32_e32 v2, v2
	v_exp_f32_e32 v3, v3
	v_exp_f32_e32 v4, v4
	v_exp_f32_e32 v5, v5
	v_exp_f32_e32 v6, v6
	v_exp_f32_e32 v7, v7
	v_exp_f32_e32 v8, v8
	v_exp_f32_e32 v9, v9
	v_pk_add_f32 v[2:3], v[2:3], vcc op_sel:[0,1] op_sel_hi:[1,1]
	v_pk_add_f32 v[4:5], v[4:5], vcc op_sel:[0,1] op_sel_hi:[1,1]
	v_pk_add_f32 v[6:7], v[6:7], vcc op_sel:[0,1] op_sel_hi:[1,1]
	v_pk_add_f32 v[8:9], v[8:9], vcc op_sel:[0,1] op_sel_hi:[1,1]
	v_rcp_f32_e32 v2, v2
	v_rcp_f32_e32 v3, v3
	v_rcp_f32_e32 v4, v4
	v_rcp_f32_e32 v5, v5
	v_rcp_f32_e32 v6, v6
	v_rcp_f32_e32 v7, v7
	v_rcp_f32_e32 v8, v8
	v_rcp_f32_e32 v9, v9
	v_pk_mul_f32 v[70:71], v[70:71], v[2:3]
	v_pk_mul_f32 v[72:73], v[72:73], v[4:5]
	v_pk_mul_f32 v[66:67], v[66:67], v[6:7]
	v_pk_mul_f32 v[68:69], v[68:69], v[8:9]
	v_pk_mul_f32 v[70:71], v[74:75], v[70:71]
	v_pk_mul_f32 v[72:73], v[76:77], v[72:73]
	v_pk_mul_f32 v[66:67], v[78:79], v[66:67]
	v_pk_mul_f32 v[68:69], v[80:81], v[68:69]
	v_med3_f32 v70, v70, s56, v219
	v_med3_f32 v71, v71, s56, v219
	v_med3_f32 v72, v72, s56, v219
	v_med3_f32 v73, v73, s56, v219
	v_med3_f32 v66, v66, s56, v219
	v_med3_f32 v67, v67, s56, v219
	v_med3_f32 v68, v68, s56, v219
	v_med3_f32 v69, v69, s56, v219
	v_cvt_pk_fp8_f32 v18, v70, v71
	v_cvt_pk_fp8_f32 v19, v66, v67
	v_cvt_pk_fp8_f32 v18, v72, v73 op_sel:[0,0,1]
	v_cvt_pk_fp8_f32 v19, v68, v69 op_sel:[0,0,1]
	s_nop 1
	v_permlane16_swap_b32_e32 v16, v18
	v_permlane16_swap_b32_e32 v17, v19
	v_add_u32_e32 v14, 0x28000, v15
	global_store_dwordx4 v14, v[16:19], s[94:95]
	s_andn2_b64 vcc, exec, s[12:13]
	s_mov_b64 s[12:13], -1
	s_cbranch_vccnz .LBB0_835
	s_andn2_b64 vcc, exec, s[4:5]
	s_cbranch_vccnz .LBB0_834
	s_barrier
	s_branch .LBB0_834

; DI float silu_f(float a) { return a * __builtin_amdgcn_rcpf(1.0f + __expf(-a)); }
;     DI void operator()(const f32x4 (&acc)[2][2][4][2], const Unit& u, int wr, int wc, int fr, int fq) const {
;         const int row0 = u.pm * 256 + wr * 64 + fr, col0 = (u.pn % pn_mod) * 128 + wc * 32 + 8 * fq;
; #pragma unroll
;         for (int ai = 0; ai < 2; ++ai)
; #pragma unroll
;             for (int m = 0; m < 4; ++m) {
;                 unsigned char* rowp = O + (size_t)(row0 + ai * 128 + m * 16) * ldc + col0;
;                 f32x4 a0 = acc[ai][0][m][0] * W8_INV, a1 = acc[ai][0][m][1] * W8_INV; const f32x4 b0 = acc[ai][1][m][0] * W8_INV, b1 = acc[ai][1][m][1] * W8_INV;
; #pragma unroll
;                 for (int j = 0; j < 4; ++j) { a0[j] = silu_f(a0[j]); a1[j] = silu_f(a1[j]); }
;                 const f32x4 v0 = a0 * b0, v1 = a1 * b1;
;                 u32x2 w; w.x = pk4_fp8(v0[0], v0[1], v0[2], v0[3]); w.y = pk4_fp8(v1[0], v1[1], v1[2], v1[3]);
;                 *(u32x2*)rowp = w;
;             }
;     }
.LBB0_1893:
	s_mov_b32 vcc_lo, 0xbfb8aa3b
	s_mov_b32 vcc_hi, 1.0
	v_and_b32_e32 v14, 8, v205
	v_lshlrev_b32_e32 v14, 1, v14
	v_add_u32_e32 v14, v14, v195
	v_lshl_add_u32 v14, s50, 8, v14
	v_lshlrev_b32_e32 v15, 10, v14
	s_and_b32 s13, s18, 7
	s_lshl_b32 s13, s13, 7
	v_and_b32_e32 v14, 0x70, v205
	v_or_b32_e32 v14, s13, v14
	v_add_u32_e32 v15, v15, v14
	v_pk_mul_f32 v[190:191], v[190:191], s[10:11] op_sel_hi:[1,0]
	v_pk_mul_f32 v[192:193], v[192:193], s[10:11] op_sel_hi:[1,0]
	v_pk_mul_f32 v[186:187], v[186:187], s[10:11] op_sel_hi:[1,0]
	v_pk_mul_f32 v[188:189], v[188:189], s[10:11] op_sel_hi:[1,0]
	v_pk_mul_f32 v[182:183], v[182:183], s[10:11] op_sel_hi:[1,0]
	v_pk_mul_f32 v[184:185], v[184:185], s[10:11] op_sel_hi:[1,0]
	v_pk_mul_f32 v[178:179], v[178:179], s[10:11] op_sel_hi:[1,0]
	v_pk_mul_f32 v[180:181], v[180:181], s[10:11] op_sel_hi:[1,0]
	v_pk_mul_f32 v[2:3], v[190:191], vcc op_sel_hi:[1,0]
	v_pk_mul_f32 v[4:5], v[192:193], vcc op_sel_hi:[1,0]
	v_pk_mul_f32 v[6:7], v[186:187], vcc op_sel_hi:[1,0]
	v_pk_mul_f32 v[8:9], v[188:189], vcc op_sel_hi:[1,0]
	v_exp_f32_e32 v2, v2
	v_exp_f32_e32 v3, v3
	v_exp_f32_e32 v4, v4
	v_exp_f32_e32 v5, v5
	v_exp_f32_e32 v6, v6
	v_exp_f32_e32 v7, v7
	v_exp_f32_e32 v8, v8
	v_exp_f32_e32 v9, v9
	v_pk_add_f32 v[2:3], v[2:3], vcc op_sel:[0,1] op_sel_hi:[1,1]
	v_pk_add_f32 v[4:5], v[4:5], vcc op_sel:[0,1] op_sel_hi:[1,1]
	v_pk_add_f32 v[6:7], v[6:7], vcc op_sel:[0,1] op_sel_hi:[1,1]
	v_pk_add_f32 v[8:9], v[8:9], vcc op_sel:[0,1] op_sel_hi:[1,1]
	v_rcp_f32_e32 v2, v2
	v_rcp_f32_e32 v3, v3
	v_rcp_f32_e32 v4, v4
	v_rcp_f32_e32 v5, v5
	v_rcp_f32_e32 v6, v6
	v_rcp_f32_e32 v7, v7
	v_rcp_f32_e32 v8, v8
	v_rcp_f32_e32 v9, v9
	v_pk_mul_f32 v[190:191], v[190:191], v[2:3]
	v_pk_mul_f32 v[192:193], v[192:193], v[4:5]
	v_pk_mul_f32 v[186:187], v[186:187], v[6:7]
	v_pk_mul_f32 v[188:189], v[188:189], v[8:9]
	v_pk_mul_f32 v[190:191], v[182:183], v[190:191]
	v_pk_mul_f32 v[192:193], v[184:185], v[192:193]
	v_pk_mul_f32 v[186:187], v[178:179], v[186:187]
	v_pk_mul_f32 v[188:189], v[180:181], v[188:189]
	v_med3_f32 v190, v190, s45, v216
	v_med3_f32 v191, v191, s45, v216
	v_med3_f32 v192, v192, s45, v216
	v_med3_f32 v193, v193, s45, v216
	v_med3_f32 v186, v186, s45, v216
	v_med3_f32 v187, v187, s45, v216
	v_med3_f32 v188, v188, s45, v216
	v_med3_f32 v189, v189, s45, v216
	v_cvt_pk_fp8_f32 v10, v190, v191
	v_cvt_pk_fp8_f32 v11, v186, v187
	v_cvt_pk_fp8_f32 v10, v192, v193 op_sel:[0,0,1]
	v_cvt_pk_fp8_f32 v11, v188, v189 op_sel:[0,0,1]
	v_pk_mul_f32 v[174:175], v[174:175], s[10:11] op_sel_hi:[1,0]
	v_pk_mul_f32 v[176:177], v[176:177], s[10:11] op_sel_hi:[1,0]
	v_pk_mul_f32 v[170:171], v[170:171], s[10:11] op_sel_hi:[1,0]
	v_pk_mul_f32 v[172:173], v[172:173], s[10:11] op_sel_hi:[1,0]
	v_pk_mul_f32 v[166:167], v[166:167], s[10:11] op_sel_hi:[1,0]
	v_pk_mul_f32 v[168:169], v[168:169], s[10:11] op_sel_hi:[1,0]
	v_pk_mul_f32 v[162:163], v[162:163], s[10:11] op_sel_hi:[1,0]
	v_pk_mul_f32 v[164:165], v[164:165], s[10:11] op_sel_hi:[1,0]
	v_pk_mul_f32 v[2:3], v[174:175], vcc op_sel_hi:[1,0]
	v_pk_mul_f32 v[4:5], v[176:177], vcc op_sel_hi:[1,0]
	v_pk_mul_f32 v[6:7], v[170:171], vcc op_sel_hi:[1,0]
	v_pk_mul_f32 v[8:9], v[172:173], vcc op_sel_hi:[1,0]
	v_exp_f32_e32 v2, v2
	v_exp_f32_e32 v3, v3
	v_exp_f32_e32 v4, v4
	v_exp_f32_e32 v5, v5
	v_exp_f32_e32 v6, v6
	v_exp_f32_e32 v7, v7
	v_exp_f32_e32 v8, v8
	v_exp_f32_e32 v9, v9
	v_pk_add_f32 v[2:3], v[2:3], vcc op_sel:[0,1] op_sel_hi:[1,1]
	v_pk_add_f32 v[4:5], v[4:5], vcc op_sel:[0,1] op_sel_hi:[1,1]
	v_pk_add_f32 v[6:7], v[6:7], vcc op_sel:[0,1] op_sel_hi:[1,1]
	v_pk_add_f32 v[8:9], v[8:9], vcc op_sel:[0,1] op_sel_hi:[1,1]
	v_rcp_f32_e32 v2, v2
	v_rcp_f32_e32 v3, v3
	v_rcp_f32_e32 v4, v4
	v_rcp_f32_e32 v5, v5
	v_rcp_f32_e32 v6, v6
	v_rcp_f32_e32 v7, v7
	v_rcp_f32_e32 v8, v8
	v_rcp_f32_e32 v9, v9
	v_pk_mul_f32 v[174:175], v[174:175], v[2:3]
	v_pk_mul_f32 v[176:177], v[176:177], v[4:5]
	v_pk_mul_f32 v[170:171], v[170:171], v[6:7]
	v_pk_mul_f32 v[172:173], v[172:173], v[8:9]
	v_pk_mul_f32 v[174:175], v[166:167], v[174:175]
	v_pk_mul_f32 v[176:177], v[168:169], v[176:177]
	v_pk_mul_f32 v[170:171], v[162:163], v[170:171]
	v_pk_mul_f32 v[172:173], v[164:165], v[172:173]
	v_med3_f32 v174, v174, s45, v216
	v_med3_f32 v175, v175, s45, v216
	v_med3_f32 v176, v176, s45, v216
	v_med3_f32 v177, v177, s45, v216
	v_med3_f32 v170, v170, s45, v216
	v_med3_f32 v171, v171, s45, v216
	v_med3_f32 v172, v172, s45, v216
	v_med3_f32 v173, v173, s45, v216
	v_cvt_pk_fp8_f32 v12, v174, v175
	v_cvt_pk_fp8_f32 v13, v170, v171
	v_cvt_pk_fp8_f32 v12, v176, v177 op_sel:[0,0,1]
	v_cvt_pk_fp8_f32 v13, v172, v173 op_sel:[0,0,1]
	s_nop 1
	v_permlane16_swap_b32_e32 v10, v12
	v_permlane16_swap_b32_e32 v11, v13
	v_mov_b32_e32 v14, v15
	global_store_dwordx4 v14, v[10:13], s[94:95]
	v_pk_mul_f32 v[158:159], v[158:159], s[10:11] op_sel_hi:[1,0]
	v_pk_mul_f32 v[160:161], v[160:161], s[10:11] op_sel_hi:[1,0]
	v_pk_mul_f32 v[154:155], v[154:155], s[10:11] op_sel_hi:[1,0]
	v_pk_mul_f32 v[156:157], v[156:157], s[10:11] op_sel_hi:[1,0]
	v_pk_mul_f32 v[150:151], v[150:151], s[10:11] op_sel_hi:[1,0]
	v_pk_mul_f32 v[152:153], v[152:153], s[10:11] op_sel_hi:[1,0]
	v_pk_mul_f32 v[146:147], v[146:147], s[10:11] op_sel_hi:[1,0]
	v_pk_mul_f32 v[148:149], v[148:149], s[10:11] op_sel_hi:[1,0]
	v_pk_mul_f32 v[2:3], v[158:159], vcc op_sel_hi:[1,0]
	v_pk_mul_f32 v[4:5], v[160:161], vcc op_sel_hi:[1,0]
	v_pk_mul_f32 v[6:7], v[154:155], vcc op_sel_hi:[1,0]
	v_pk_mul_f32 v[8:9], v[156:157], vcc op_sel_hi:[1,0]
	v_exp_f32_e32 v2, v2
	v_exp_f32_e32 v3, v3
	v_exp_f32_e32 v4, v4
	v_exp_f32_e32 v5, v5
	v_exp_f32_e32 v6, v6
	v_exp_f32_e32 v7, v7
; DI unsigned pk4_fp8(float a, float b, float c, float d) {
;     a = __builtin_amdgcn_fmed3f(a, -448.0f, 448.0f); b = __builtin_amdgcn_fmed3f(b, -448.0f, 448.0f); c = __builtin_amdgcn_fmed3f(c, -448.0f, 448.0f); d = __builtin_amdgcn_fmed3f(d, -448.0f, 448.0f);
;     int w = __builtin_amdgcn_cvt_pk_fp8_f32(a, b, 0, false); w = __builtin_amdgcn_cvt_pk_fp8_f32(c, d, w, true); return (unsigned)w;
; }
; DI f32x4 unpk4_fp8(unsigned w) { const f32x2 lo = __builtin_amdgcn_cvt_pk_f32_fp8((int)w, false), hi = __builtin_amdgcn_cvt_pk_f32_fp8((int)w, true); return (f32x4){lo.x, lo.y, hi.x, hi.y}; }
; DI float silu_f(float a) { return a * __builtin_amdgcn_rcpf(1.0f + __expf(-a)); }
;     DI void operator()(const f32x4 (&acc)[2][2][4][2], const Unit& u, int wr, int wc, int fr, int fq) const {
;         const int row0 = u.pm * 256 + wr * 64 + fr, col0 = (u.pn % pn_mod) * 128 + wc * 32 + 8 * fq;
; #pragma unroll
;         for (int ai = 0; ai < 2; ++ai)
; #pragma unroll
;             for (int m = 0; m < 4; ++m) {
;                 unsigned char* rowp = O + (size_t)(row0 + ai * 128 + m * 16) * ldc + col0;
;                 f32x4 a0 = acc[ai][0][m][0] * W8_INV, a1 = acc[ai][0][m][1] * W8_INV; const f32x4 b0 = acc[ai][1][m][0] * W8_INV, b1 = acc[ai][1][m][1] * W8_INV;
; #pragma unroll
;                 for (int j = 0; j < 4; ++j) { a0[j] = silu_f(a0[j]); a1[j] = silu_f(a1[j]); }
;                 const f32x4 v0 = a0 * b0, v1 = a1 * b1;
;                 u32x2 w; w.x = pk4_fp8(v0[0], v0[1], v0[2], v0[3]); w.y = pk4_fp8(v1[0], v1[1], v1[2], v1[3]);
;                 *(u32x2*)rowp = w;
;             }
	v_exp_f32_e32 v8, v8
	v_exp_f32_e32 v9, v9
	v_pk_add_f32 v[2:3], v[2:3], vcc op_sel:[0,1] op_sel_hi:[1,1]
	v_pk_add_f32 v[4:5], v[4:5], vcc op_sel:[0,1] op_sel_hi:[1,1]
	v_pk_add_f32 v[6:7], v[6:7], vcc op_sel:[0,1] op_sel_hi:[1,1]
	v_pk_add_f32 v[8:9], v[8:9], vcc op_sel:[0,1] op_sel_hi:[1,1]
	v_rcp_f32_e32 v2, v2
	v_rcp_f32_e32 v3, v3
	v_rcp_f32_e32 v4, v4
	v_rcp_f32_e32 v5, v5
	v_rcp_f32_e32 v6, v6
	v_rcp_f32_e32 v7, v7
	v_rcp_f32_e32 v8, v8
	v_rcp_f32_e32 v9, v9
	v_pk_mul_f32 v[158:159], v[158:159], v[2:3]
	v_pk_mul_f32 v[160:161], v[160:161], v[4:5]
	v_pk_mul_f32 v[154:155], v[154:155], v[6:7]
	v_pk_mul_f32 v[156:157], v[156:157], v[8:9]
	v_pk_mul_f32 v[158:159], v[150:151], v[158:159]
	v_pk_mul_f32 v[160:161], v[152:153], v[160:161]
	v_pk_mul_f32 v[154:155], v[146:147], v[154:155]
	v_pk_mul_f32 v[156:157], v[148:149], v[156:157]
	v_med3_f32 v158, v158, s45, v216
	v_med3_f32 v159, v159, s45, v216
	v_med3_f32 v160, v160, s45, v216
	v_med3_f32 v161, v161, s45, v216
	v_med3_f32 v154, v154, s45, v216
	v_med3_f32 v155, v155, s45, v216
	v_med3_f32 v156, v156, s45, v216
	v_med3_f32 v157, v157, s45, v216
	v_cvt_pk_fp8_f32 v16, v158, v159
	v_cvt_pk_fp8_f32 v17, v154, v155
	v_cvt_pk_fp8_f32 v16, v160, v161 op_sel:[0,0,1]
	v_cvt_pk_fp8_f32 v17, v156, v157 op_sel:[0,0,1]
	v_pk_mul_f32 v[142:143], v[142:143], s[10:11] op_sel_hi:[1,0]
	v_pk_mul_f32 v[144:145], v[144:145], s[10:11] op_sel_hi:[1,0]
	v_pk_mul_f32 v[138:139], v[138:139], s[10:11] op_sel_hi:[1,0]
	v_pk_mul_f32 v[140:141], v[140:141], s[10:11] op_sel_hi:[1,0]
	v_pk_mul_f32 v[134:135], v[134:135], s[10:11] op_sel_hi:[1,0]
	v_pk_mul_f32 v[136:137], v[136:137], s[10:11] op_sel_hi:[1,0]
	v_pk_mul_f32 v[130:131], v[130:131], s[10:11] op_sel_hi:[1,0]
	v_pk_mul_f32 v[132:133], v[132:133], s[10:11] op_sel_hi:[1,0]
	v_pk_mul_f32 v[2:3], v[142:143], vcc op_sel_hi:[1,0]
	v_pk_mul_f32 v[4:5], v[144:145], vcc op_sel_hi:[1,0]
	v_pk_mul_f32 v[6:7], v[138:139], vcc op_sel_hi:[1,0]
	v_pk_mul_f32 v[8:9], v[140:141], vcc op_sel_hi:[1,0]
	v_exp_f32_e32 v2, v2
	v_exp_f32_e32 v3, v3
	v_exp_f32_e32 v4, v4
	v_exp_f32_e32 v5, v5
	v_exp_f32_e32 v6, v6
	v_exp_f32_e32 v7, v7
	v_exp_f32_e32 v8, v8
	v_exp_f32_e32 v9, v9
	v_pk_add_f32 v[2:3], v[2:3], vcc op_sel:[0,1] op_sel_hi:[1,1]
	v_pk_add_f32 v[4:5], v[4:5], vcc op_sel:[0,1] op_sel_hi:[1,1]
	v_pk_add_f32 v[6:7], v[6:7], vcc op_sel:[0,1] op_sel_hi:[1,1]
	v_pk_add_f32 v[8:9], v[8:9], vcc op_sel:[0,1] op_sel_hi:[1,1]
	v_rcp_f32_e32 v2, v2
	v_rcp_f32_e32 v3, v3
	v_rcp_f32_e32 v4, v4
	v_rcp_f32_e32 v5, v5
	v_rcp_f32_e32 v6, v6
	v_rcp_f32_e32 v7, v7
	v_rcp_f32_e32 v8, v8
	v_rcp_f32_e32 v9, v9
	v_pk_mul_f32 v[142:143], v[142:143], v[2:3]
	v_pk_mul_f32 v[144:145], v[144:145], v[4:5]
	v_pk_mul_f32 v[138:139], v[138:139], v[6:7]
	v_pk_mul_f32 v[140:141], v[140:141], v[8:9]
	v_pk_mul_f32 v[142:143], v[134:135], v[142:143]
	v_pk_mul_f32 v[144:145], v[136:137], v[144:145]
	v_pk_mul_f32 v[138:139], v[130:131], v[138:139]
	v_pk_mul_f32 v[140:141], v[132:133], v[140:141]
	v_med3_f32 v142, v142, s45, v216
	v_med3_f32 v143, v143, s45, v216
	v_med3_f32 v144, v144, s45, v216
	v_med3_f32 v145, v145, s45, v216
	v_med3_f32 v138, v138, s45, v216
	v_med3_f32 v139, v139, s45, v216
	v_med3_f32 v140, v140, s45, v216
	v_med3_f32 v141, v141, s45, v216
	v_cvt_pk_fp8_f32 v18, v142, v143
	v_cvt_pk_fp8_f32 v19, v138, v139
	v_cvt_pk_fp8_f32 v18, v144, v145 op_sel:[0,0,1]
	v_cvt_pk_fp8_f32 v19, v140, v141 op_sel:[0,0,1]
	s_nop 1
	v_permlane16_swap_b32_e32 v16, v18
	v_permlane16_swap_b32_e32 v17, v19
	v_add_u32_e32 v14, 0x8000, v15
	global_store_dwordx4 v14, v[16:19], s[94:95]
	v_pk_mul_f32 v[126:127], v[126:127], s[10:11] op_sel_hi:[1,0]
	v_pk_mul_f32 v[128:129], v[128:129], s[10:11] op_sel_hi:[1,0]
	v_pk_mul_f32 v[122:123], v[122:123], s[10:11] op_sel_hi:[1,0]
	v_pk_mul_f32 v[124:125], v[124:125], s[10:11] op_sel_hi:[1,0]
	v_pk_mul_f32 v[118:119], v[118:119], s[10:11] op_sel_hi:[1,0]
	v_pk_mul_f32 v[120:121], v[120:121], s[10:11] op_sel_hi:[1,0]
	v_pk_mul_f32 v[114:115], v[114:115], s[10:11] op_sel_hi:[1,0]
	v_pk_mul_f32 v[116:117], v[116:117], s[10:11] op_sel_hi:[1,0]
	v_pk_mul_f32 v[2:3], v[126:127], vcc op_sel_hi:[1,0]
	v_pk_mul_f32 v[4:5], v[128:129], vcc op_sel_hi:[1,0]
	v_pk_mul_f32 v[6:7], v[122:123], vcc op_sel_hi:[1,0]
	v_pk_mul_f32 v[8:9], v[124:125], vcc op_sel_hi:[1,0]
	v_exp_f32_e32 v2, v2
	v_exp_f32_e32 v3, v3
	v_exp_f32_e32 v4, v4
	v_exp_f32_e32 v5, v5
	v_exp_f32_e32 v6, v6
	v_exp_f32_e32 v7, v7
	v_exp_f32_e32 v8, v8
	v_exp_f32_e32 v9, v9
	v_pk_add_f32 v[2:3], v[2:3], vcc op_sel:[0,1] op_sel_hi:[1,1]
	v_pk_add_f32 v[4:5], v[4:5], vcc op_sel:[0,1] op_sel_hi:[1,1]
	v_pk_add_f32 v[6:7], v[6:7], vcc op_sel:[0,1] op_sel_hi:[1,1]
	v_pk_add_f32 v[8:9], v[8:9], vcc op_sel:[0,1] op_sel_hi:[1,1]
	v_rcp_f32_e32 v2, v2
	v_rcp_f32_e32 v3, v3
	v_rcp_f32_e32 v4, v4
	v_rcp_f32_e32 v5, v5
	v_rcp_f32_e32 v6, v6
	v_rcp_f32_e32 v7, v7
	v_rcp_f32_e32 v8, v8
	v_rcp_f32_e32 v9, v9
	v_pk_mul_f32 v[126:127], v[126:127], v[2:3]
	v_pk_mul_f32 v[128:129], v[128:129], v[4:5]
	v_pk_mul_f32 v[122:123], v[122:123], v[6:7]
	v_pk_mul_f32 v[124:125], v[124:125], v[8:9]
	v_pk_mul_f32 v[126:127], v[118:119], v[126:127]
	v_pk_mul_f32 v[128:129], v[120:121], v[128:129]
	v_pk_mul_f32 v[122:123], v[114:115], v[122:123]
	v_pk_mul_f32 v[124:125], v[116:117], v[124:125]
	v_med3_f32 v126, v126, s45, v216
	v_med3_f32 v127, v127, s45, v216
	v_med3_f32 v128, v128, s45, v216
	v_med3_f32 v129, v129, s45, v216
	v_med3_f32 v122, v122, s45, v216
	v_med3_f32 v123, v123, s45, v216
	v_med3_f32 v124, v124, s45, v216
	v_med3_f32 v125, v125, s45, v216
	v_cvt_pk_fp8_f32 v10, v126, v127
	v_cvt_pk_fp8_f32 v11, v122, v123
; DI unsigned pk4_fp8(float a, float b, float c, float d) {
;     a = __builtin_amdgcn_fmed3f(a, -448.0f, 448.0f); b = __builtin_amdgcn_fmed3f(b, -448.0f, 448.0f); c = __builtin_amdgcn_fmed3f(c, -448.0f, 448.0f); d = __builtin_amdgcn_fmed3f(d, -448.0f, 448.0f);
;     int w = __builtin_amdgcn_cvt_pk_fp8_f32(a, b, 0, false); w = __builtin_amdgcn_cvt_pk_fp8_f32(c, d, w, true); return (unsigned)w;
; }
; DI f32x4 unpk4_fp8(unsigned w) { const f32x2 lo = __builtin_amdgcn_cvt_pk_f32_fp8((int)w, false), hi = __builtin_amdgcn_cvt_pk_f32_fp8((int)w, true); return (f32x4){lo.x, lo.y, hi.x, hi.y}; }
; DI float silu_f(float a) { return a * __builtin_amdgcn_rcpf(1.0f + __expf(-a)); }
;     DI void operator()(const f32x4 (&acc)[2][2][4][2], const Unit& u, int wr, int wc, int fr, int fq) const {
;         const int row0 = u.pm * 256 + wr * 64 + fr, col0 = (u.pn % pn_mod) * 128 + wc * 32 + 8 * fq;
; #pragma unroll
;         for (int ai = 0; ai < 2; ++ai)
; #pragma unroll
;             for (int m = 0; m < 4; ++m) {
;                 unsigned char* rowp = O + (size_t)(row0 + ai * 128 + m * 16) * ldc + col0;
;                 f32x4 a0 = acc[ai][0][m][0] * W8_INV, a1 = acc[ai][0][m][1] * W8_INV; const f32x4 b0 = acc[ai][1][m][0] * W8_INV, b1 = acc[ai][1][m][1] * W8_INV;
; #pragma unroll
;                 for (int j = 0; j < 4; ++j) { a0[j] = silu_f(a0[j]); a1[j] = silu_f(a1[j]); }
;                 const f32x4 v0 = a0 * b0, v1 = a1 * b1;
;                 u32x2 w; w.x = pk4_fp8(v0[0], v0[1], v0[2], v0[3]); w.y = pk4_fp8(v1[0], v1[1], v1[2], v1[3]);
;                 *(u32x2*)rowp = w;
;             }
	v_cvt_pk_fp8_f32 v10, v128, v129 op_sel:[0,0,1]
	v_cvt_pk_fp8_f32 v11, v124, v125 op_sel:[0,0,1]
	v_pk_mul_f32 v[110:111], v[110:111], s[10:11] op_sel_hi:[1,0]
	v_pk_mul_f32 v[112:113], v[112:113], s[10:11] op_sel_hi:[1,0]
	v_pk_mul_f32 v[106:107], v[106:107], s[10:11] op_sel_hi:[1,0]
	v_pk_mul_f32 v[108:109], v[108:109], s[10:11] op_sel_hi:[1,0]
	v_pk_mul_f32 v[94:95], v[94:95], s[10:11] op_sel_hi:[1,0]
	v_pk_mul_f32 v[96:97], v[96:97], s[10:11] op_sel_hi:[1,0]
	v_pk_mul_f32 v[86:87], v[86:87], s[10:11] op_sel_hi:[1,0]
	v_pk_mul_f32 v[88:89], v[88:89], s[10:11] op_sel_hi:[1,0]
	v_pk_mul_f32 v[2:3], v[110:111], vcc op_sel_hi:[1,0]
	v_pk_mul_f32 v[4:5], v[112:113], vcc op_sel_hi:[1,0]
	v_pk_mul_f32 v[6:7], v[106:107], vcc op_sel_hi:[1,0]
	v_pk_mul_f32 v[8:9], v[108:109], vcc op_sel_hi:[1,0]
	v_exp_f32_e32 v2, v2
	v_exp_f32_e32 v3, v3
	v_exp_f32_e32 v4, v4
	v_exp_f32_e32 v5, v5
	v_exp_f32_e32 v6, v6
	v_exp_f32_e32 v7, v7
	v_exp_f32_e32 v8, v8
	v_exp_f32_e32 v9, v9
	v_pk_add_f32 v[2:3], v[2:3], vcc op_sel:[0,1] op_sel_hi:[1,1]
	v_pk_add_f32 v[4:5], v[4:5], vcc op_sel:[0,1] op_sel_hi:[1,1]
	v_pk_add_f32 v[6:7], v[6:7], vcc op_sel:[0,1] op_sel_hi:[1,1]
	v_pk_add_f32 v[8:9], v[8:9], vcc op_sel:[0,1] op_sel_hi:[1,1]
	v_rcp_f32_e32 v2, v2
	v_rcp_f32_e32 v3, v3
	v_rcp_f32_e32 v4, v4
	v_rcp_f32_e32 v5, v5
	v_rcp_f32_e32 v6, v6
	v_rcp_f32_e32 v7, v7
	v_rcp_f32_e32 v8, v8
	v_rcp_f32_e32 v9, v9
	v_pk_mul_f32 v[110:111], v[110:111], v[2:3]
	v_pk_mul_f32 v[112:113], v[112:113], v[4:5]
	v_pk_mul_f32 v[106:107], v[106:107], v[6:7]
	v_pk_mul_f32 v[108:109], v[108:109], v[8:9]
	v_pk_mul_f32 v[110:111], v[94:95], v[110:111]
	v_pk_mul_f32 v[112:113], v[96:97], v[112:113]
	v_pk_mul_f32 v[106:107], v[86:87], v[106:107]
	v_pk_mul_f32 v[108:109], v[88:89], v[108:109]
	v_med3_f32 v110, v110, s45, v216
	v_med3_f32 v111, v111, s45, v216
	v_med3_f32 v112, v112, s45, v216
	v_med3_f32 v113, v113, s45, v216
	v_med3_f32 v106, v106, s45, v216
	v_med3_f32 v107, v107, s45, v216
	v_med3_f32 v108, v108, s45, v216
	v_med3_f32 v109, v109, s45, v216
	v_cvt_pk_fp8_f32 v12, v110, v111
	v_cvt_pk_fp8_f32 v13, v106, v107
	v_cvt_pk_fp8_f32 v12, v112, v113 op_sel:[0,0,1]
	v_cvt_pk_fp8_f32 v13, v108, v109 op_sel:[0,0,1]
	s_nop 1
	v_permlane16_swap_b32_e32 v10, v12
	v_permlane16_swap_b32_e32 v11, v13
	v_add_u32_e32 v14, 0x20000, v15
	global_store_dwordx4 v14, v[10:13], s[94:95]
	v_pk_mul_f32 v[90:91], v[90:91], s[10:11] op_sel_hi:[1,0]
	v_pk_mul_f32 v[92:93], v[92:93], s[10:11] op_sel_hi:[1,0]
	v_pk_mul_f32 v[82:83], v[82:83], s[10:11] op_sel_hi:[1,0]
	v_pk_mul_f32 v[84:85], v[84:85], s[10:11] op_sel_hi:[1,0]
	v_pk_mul_f32 v[98:99], v[98:99], s[10:11] op_sel_hi:[1,0]
	v_pk_mul_f32 v[100:101], v[100:101], s[10:11] op_sel_hi:[1,0]
	v_pk_mul_f32 v[102:103], v[102:103], s[10:11] op_sel_hi:[1,0]
	v_pk_mul_f32 v[104:105], v[104:105], s[10:11] op_sel_hi:[1,0]
	v_pk_mul_f32 v[2:3], v[90:91], vcc op_sel_hi:[1,0]
	v_pk_mul_f32 v[4:5], v[92:93], vcc op_sel_hi:[1,0]
	v_pk_mul_f32 v[6:7], v[82:83], vcc op_sel_hi:[1,0]
	v_pk_mul_f32 v[8:9], v[84:85], vcc op_sel_hi:[1,0]
	v_exp_f32_e32 v2, v2
	v_exp_f32_e32 v3, v3
	v_exp_f32_e32 v4, v4
	v_exp_f32_e32 v5, v5
	v_exp_f32_e32 v6, v6
	v_exp_f32_e32 v7, v7
	v_exp_f32_e32 v8, v8
	v_exp_f32_e32 v9, v9
	v_pk_add_f32 v[2:3], v[2:3], vcc op_sel:[0,1] op_sel_hi:[1,1]
	v_pk_add_f32 v[4:5], v[4:5], vcc op_sel:[0,1] op_sel_hi:[1,1]
	v_pk_add_f32 v[6:7], v[6:7], vcc op_sel:[0,1] op_sel_hi:[1,1]
	v_pk_add_f32 v[8:9], v[8:9], vcc op_sel:[0,1] op_sel_hi:[1,1]
	v_rcp_f32_e32 v2, v2
	v_rcp_f32_e32 v3, v3
	v_rcp_f32_e32 v4, v4
	v_rcp_f32_e32 v5, v5
	v_rcp_f32_e32 v6, v6
	v_rcp_f32_e32 v7, v7
	v_rcp_f32_e32 v8, v8
	v_rcp_f32_e32 v9, v9
	v_pk_mul_f32 v[90:91], v[90:91], v[2:3]
	v_pk_mul_f32 v[92:93], v[92:93], v[4:5]
	v_pk_mul_f32 v[82:83], v[82:83], v[6:7]
	v_pk_mul_f32 v[84:85], v[84:85], v[8:9]
	v_pk_mul_f32 v[90:91], v[98:99], v[90:91]
	v_pk_mul_f32 v[92:93], v[100:101], v[92:93]
	v_pk_mul_f32 v[82:83], v[102:103], v[82:83]
	v_pk_mul_f32 v[84:85], v[104:105], v[84:85]
	v_med3_f32 v90, v90, s45, v216
	v_med3_f32 v91, v91, s45, v216
	v_med3_f32 v92, v92, s45, v216
	v_med3_f32 v93, v93, s45, v216
	v_med3_f32 v82, v82, s45, v216
	v_med3_f32 v83, v83, s45, v216
	v_med3_f32 v84, v84, s45, v216
	v_med3_f32 v85, v85, s45, v216
	v_cvt_pk_fp8_f32 v16, v90, v91
	v_cvt_pk_fp8_f32 v17, v82, v83
	v_cvt_pk_fp8_f32 v16, v92, v93 op_sel:[0,0,1]
	v_cvt_pk_fp8_f32 v17, v84, v85 op_sel:[0,0,1]
	v_pk_mul_f32 v[70:71], v[70:71], s[10:11] op_sel_hi:[1,0]
	v_pk_mul_f32 v[72:73], v[72:73], s[10:11] op_sel_hi:[1,0]
	v_pk_mul_f32 v[66:67], v[66:67], s[10:11] op_sel_hi:[1,0]
	v_pk_mul_f32 v[68:69], v[68:69], s[10:11] op_sel_hi:[1,0]
	v_pk_mul_f32 v[74:75], v[74:75], s[10:11] op_sel_hi:[1,0]
	v_pk_mul_f32 v[76:77], v[76:77], s[10:11] op_sel_hi:[1,0]
	v_pk_mul_f32 v[78:79], v[78:79], s[10:11] op_sel_hi:[1,0]
	v_pk_mul_f32 v[80:81], v[80:81], s[10:11] op_sel_hi:[1,0]
	v_pk_mul_f32 v[2:3], v[70:71], vcc op_sel_hi:[1,0]
	v_pk_mul_f32 v[4:5], v[72:73], vcc op_sel_hi:[1,0]
	v_pk_mul_f32 v[6:7], v[66:67], vcc op_sel_hi:[1,0]
	v_pk_mul_f32 v[8:9], v[68:69], vcc op_sel_hi:[1,0]
	v_exp_f32_e32 v2, v2
	v_exp_f32_e32 v3, v3
	v_exp_f32_e32 v4, v4
	v_exp_f32_e32 v5, v5
	v_exp_f32_e32 v6, v6
	v_exp_f32_e32 v7, v7
	v_exp_f32_e32 v8, v8
	v_exp_f32_e32 v9, v9
	v_pk_add_f32 v[2:3], v[2:3], vcc op_sel:[0,1] op_sel_hi:[1,1]
	v_pk_add_f32 v[4:5], v[4:5], vcc op_sel:[0,1] op_sel_hi:[1,1]
	v_pk_add_f32 v[6:7], v[6:7], vcc op_sel:[0,1] op_sel_hi:[1,1]
	v_pk_add_f32 v[8:9], v[8:9], vcc op_sel:[0,1] op_sel_hi:[1,1]
	v_rcp_f32_e32 v2, v2
	v_rcp_f32_e32 v3, v3
	v_rcp_f32_e32 v4, v4
	v_rcp_f32_e32 v5, v5
	v_rcp_f32_e32 v6, v6
	v_rcp_f32_e32 v7, v7
	v_rcp_f32_e32 v8, v8
	v_rcp_f32_e32 v9, v9
	v_pk_mul_f32 v[70:71], v[70:71], v[2:3]
	v_pk_mul_f32 v[72:73], v[72:73], v[4:5]
	v_pk_mul_f32 v[66:67], v[66:67], v[6:7]
	v_pk_mul_f32 v[68:69], v[68:69], v[8:9]
	v_pk_mul_f32 v[70:71], v[74:75], v[70:71]
	v_pk_mul_f32 v[72:73], v[76:77], v[72:73]
	v_pk_mul_f32 v[66:67], v[78:79], v[66:67]
	v_pk_mul_f32 v[68:69], v[80:81], v[68:69]
	v_med3_f32 v70, v70, s45, v216
	v_med3_f32 v71, v71, s45, v216
	v_med3_f32 v72, v72, s45, v216
	v_med3_f32 v73, v73, s45, v216
	v_med3_f32 v66, v66, s45, v216
	v_med3_f32 v67, v67, s45, v216
	v_med3_f32 v68, v68, s45, v216
	v_med3_f32 v69, v69, s45, v216
	v_cvt_pk_fp8_f32 v18, v70, v71
	v_cvt_pk_fp8_f32 v19, v66, v67
	v_cvt_pk_fp8_f32 v18, v72, v73 op_sel:[0,0,1]
	v_cvt_pk_fp8_f32 v19, v68, v69 op_sel:[0,0,1]
	s_nop 1
	v_permlane16_swap_b32_e32 v16, v18
	v_permlane16_swap_b32_e32 v17, v19
	v_add_u32_e32 v14, 0x28000, v15
	global_store_dwordx4 v14, v[16:19], s[94:95]
	s_andn2_b64 vcc, exec, s[14:15]
	s_mov_b64 s[14:15], -1
	s_cbranch_vccnz .LBB0_1882
	s_andn2_b64 vcc, exec, s[6:7]
	s_cbranch_vccnz .LBB0_1881
	s_barrier
	s_branch .LBB0_1881
